# baseline (speedup 1.0000x reference)
_Z11prep_kernelPKfS0_S0_S0_S0_S0_S0_S0_S0_PKiPDv8_DF16bS4_PfS5_S5_PiPt:
	s_load_dwordx4 s[16:19], s[0:1], 0x0
	s_load_dwordx4 s[20:23], s[0:1], 0x10
	s_load_dwordx4 s[24:27], s[0:1], 0x20
	s_load_dwordx4 s[28:31], s[0:1], 0x30
	s_load_dwordx4 s[32:35], s[0:1], 0x40
	s_load_dwordx2 s[36:37], s[0:1], 0x80
	v_and_b32_e32 v126, 63, v0
	v_lshrrev_b32_e32 v128, 6, v0
	v_and_b32_e32 v1, 15, v0
	v_bfe_u32 v24, v0, 4, 2
	v_lshl_or_b32 v107, v128, 4, v1
	v_lshlrev_b32_e32 v106, 2, v107
	v_lshlrev_b32_e32 v127, 2, v0
	v_lshlrev_b32_e32 v25, 1, v107
	v_and_b32_e32 v26, 48, v0
	v_mul_u32_u24_e32 v27, 0x440, v24
	v_lshlrev_b32_e32 v120, 4, v0
	v_lshrrev_b32_e32 v58, 5, v0
	v_mul_u32_u24_e32 v58, 0x110, v58
	v_and_b32_e32 v125, 31, v0
	v_lshl_add_u32 v58, v125, 3, v58
	v_add_u32_e32 v124, 0x1b400, v58
	v_mul_u32_u24_e32 v52, 0x110, v1
	v_add_u32_e32 v52, v52, v26
	v_add_u32_e32 v53, 0x1b400, v52
	v_add_u32_e32 v54, 0x1c500, v52
	v_add_u32_e32 v55, v27, v25
	v_add_u32_e32 v55, 0x1c500, v55
	v_mul_u32_u24_e32 v56, 0x110, v107
	v_add_u32_e32 v56, v56, v26
	v_add_u32_e32 v57, 0x8800, v56
	s_lshl_b32 s12, s2, 4
	s_add_i32 s3, s12, 0xfffff800
	s_cmpk_gt_i32 s2, 0x7f
	s_cselect_b64 s[6:7], -1, 0
	s_mov_b32 s48, 0
	s_mov_b32 s49, -1
	v_lshl_or_b32 v123, s2, 3, v128
	v_lshlrev_b32_e32 v123, 12, v123
	v_lshl_add_u32 v123, v126, 4, v123
	s_waitcnt lgkmcnt(0)
	s_cmpk_lt_i32 s2, 0x80
	s_cselect_b32 s38, s16, s18
	s_cselect_b32 s39, s17, s19
	s_cselect_b32 s40, s20, s24
	s_cselect_b32 s41, s21, s25
	s_cselect_b32 s13, s12, s3
	s_cselect_b32 s44, 0x3db504f3, 1.0
	s_lshl_b32 s13, s13, 9
	s_add_u32 s38, s38, s13
	s_addc_u32 s39, s39, 0
	global_load_dwordx4 v[2:5], v120, s[38:39] nt
	s_and_b32 s13, s2, 7
	s_lshl_b32 s14, s13, 13
	v_add_u32_e32 v125, s14, v120
	global_load_dwordx4 v[80:83], v125, s[40:41]
	s_add_i32 s13, s2, 1
	s_and_b32 s13, s13, 7
	s_lshl_b32 s14, s13, 13
	v_add_u32_e32 v125, s14, v120
	global_load_dwordx4 v[84:87], v125, s[40:41]
	s_add_i32 s13, s2, 2
	s_and_b32 s13, s13, 7
	s_lshl_b32 s14, s13, 13
	v_add_u32_e32 v125, s14, v120
	global_load_dwordx4 v[88:91], v125, s[40:41]
	s_add_i32 s13, s2, 3
	s_and_b32 s13, s13, 7
	s_lshl_b32 s14, s13, 13
	v_add_u32_e32 v125, s14, v120
	global_load_dwordx4 v[92:95], v125, s[40:41]
	s_add_i32 s13, s2, 4
	s_and_b32 s13, s13, 7
	s_lshl_b32 s14, s13, 13
	v_add_u32_e32 v125, s14, v120
	global_load_dwordx4 v[96:99], v125, s[40:41]
	s_add_i32 s13, s2, 5
	s_and_b32 s13, s13, 7
	s_lshl_b32 s14, s13, 13
	v_add_u32_e32 v125, s14, v120
	global_load_dwordx4 v[100:103], v125, s[40:41]
	s_add_i32 s13, s2, 6
	s_and_b32 s13, s13, 7
	s_lshl_b32 s14, s13, 13
	v_add_u32_e32 v125, s14, v120
	global_load_dwordx4 v[108:111], v125, s[40:41]
	s_add_i32 s13, s2, 7
	s_and_b32 s13, s13, 7
	s_lshl_b32 s14, s13, 13
	v_add_u32_e32 v125, s14, v120
	global_load_dwordx4 v[112:115], v125, s[40:41]
	global_load_dword v129, v106, s[32:33]
	global_load_dword v130, v106, s[30:31]
	s_and_b64 vcc, exec, s[6:7]
	s_cbranch_vccz .Lp_q
	v_cmp_gt_u32_e32 vcc, 32, v126
	v_mov_b32_e32 v198, 0x3db504f3
	v_mov_b32_e32 v125, s22
	v_mov_b32_e32 v104, s26
	v_cndmask_b32_e32 v198, 1.0, v198, vcc
	v_cndmask_b32_e32 v104, v104, v125, vcc
	v_mov_b32_e32 v125, s23
	v_mov_b32_e32 v105, s27
	v_cndmask_b32_e32 v105, v105, v125, vcc
	v_and_b32_e32 v196, 31, v126
	v_lshlrev_b32_e32 v196, 4, v196
	v_mov_b32_e32 v197, 0
	v_lshl_add_u64 v[104:105], v[104:105], 0, v[196:197]
	global_load_dwordx4 v[116:119], v[104:105], off
	v_lshlrev_b32_e32 v121, 14, v128
	v_lshl_add_u32 v121, v126, 4, v121
	s_and_b32 s13, s2, 15
	s_lshl_b32 s14, s13, 10
	s_add_u32 s46, s28, s14
	s_addc_u32 s47, s29, 0
	global_load_dwordx4 v[132:135], v121, s[46:47]
	s_add_i32 s13, s2, 1
	s_and_b32 s13, s13, 15
	s_lshl_b32 s14, s13, 10
	s_add_u32 s46, s28, s14
	s_addc_u32 s47, s29, 0
	global_load_dwordx4 v[136:139], v121, s[46:47]
	s_add_i32 s13, s2, 2
	s_and_b32 s13, s13, 15
	s_lshl_b32 s14, s13, 10
	s_add_u32 s46, s28, s14
	s_addc_u32 s47, s29, 0
	global_load_dwordx4 v[140:143], v121, s[46:47]
	s_add_i32 s13, s2, 3
	s_and_b32 s13, s13, 15
	s_lshl_b32 s14, s13, 10
	s_add_u32 s46, s28, s14
	s_addc_u32 s47, s29, 0
	global_load_dwordx4 v[144:147], v121, s[46:47]
	s_add_i32 s13, s2, 4
	s_and_b32 s13, s13, 15
	s_lshl_b32 s14, s13, 10
	s_add_u32 s46, s28, s14
	s_addc_u32 s47, s29, 0
	global_load_dwordx4 v[148:151], v121, s[46:47]
	s_add_i32 s13, s2, 5
	s_and_b32 s13, s13, 15
	s_lshl_b32 s14, s13, 10
	s_add_u32 s46, s28, s14
	s_addc_u32 s47, s29, 0
	global_load_dwordx4 v[152:155], v121, s[46:47]
	s_add_i32 s13, s2, 6
	s_and_b32 s13, s13, 15
	s_lshl_b32 s14, s13, 10
	s_add_u32 s46, s28, s14
	s_addc_u32 s47, s29, 0
	global_load_dwordx4 v[156:159], v121, s[46:47]
	s_add_i32 s13, s2, 7
	s_and_b32 s13, s13, 15
	s_lshl_b32 s14, s13, 10
	s_add_u32 s46, s28, s14
	s_addc_u32 s47, s29, 0
	global_load_dwordx4 v[160:163], v121, s[46:47]
	s_add_i32 s13, s2, 8
	s_and_b32 s13, s13, 15
	s_lshl_b32 s14, s13, 10
	s_add_u32 s46, s28, s14
	s_addc_u32 s47, s29, 0
	global_load_dwordx4 v[164:167], v121, s[46:47]
	s_add_i32 s13, s2, 9
	s_and_b32 s13, s13, 15
	s_lshl_b32 s14, s13, 10
	s_add_u32 s46, s28, s14
	s_addc_u32 s47, s29, 0
	global_load_dwordx4 v[168:171], v121, s[46:47]
	s_add_i32 s13, s2, 10
	s_and_b32 s13, s13, 15
	s_lshl_b32 s14, s13, 10
	s_add_u32 s46, s28, s14
	s_addc_u32 s47, s29, 0
	global_load_dwordx4 v[172:175], v121, s[46:47]
	s_add_i32 s13, s2, 11
	s_and_b32 s13, s13, 15
	s_lshl_b32 s14, s13, 10
	s_add_u32 s46, s28, s14
	s_addc_u32 s47, s29, 0
	global_load_dwordx4 v[176:179], v121, s[46:47]
	s_add_i32 s13, s2, 12
	s_and_b32 s13, s13, 15
	s_lshl_b32 s14, s13, 10
	s_add_u32 s46, s28, s14
	s_addc_u32 s47, s29, 0
	global_load_dwordx4 v[180:183], v121, s[46:47]
	s_add_i32 s13, s2, 13
	s_and_b32 s13, s13, 15
	s_lshl_b32 s14, s13, 10
	s_add_u32 s46, s28, s14
	s_addc_u32 s47, s29, 0
	global_load_dwordx4 v[184:187], v121, s[46:47]
	s_add_i32 s13, s2, 14
	s_and_b32 s13, s13, 15
	s_lshl_b32 s14, s13, 10
	s_add_u32 s46, s28, s14
	s_addc_u32 s47, s29, 0
	global_load_dwordx4 v[188:191], v121, s[46:47]
	s_add_i32 s13, s2, 15
	s_and_b32 s13, s13, 15
	s_lshl_b32 s14, s13, 10
	s_add_u32 s46, s28, s14
	s_addc_u32 s47, s29, 0
	global_load_dwordx4 v[192:195], v121, s[46:47]
	v_mul_u32_u24_e32 v59, 0x1040, v128
	v_lshl_add_u32 v59, v126, 2, v59
	v_add_u32_e32 v59, 0x11000, v59
	v_mul_u32_u24_e32 v76, 0x1100, v128
	v_lshl_add_u32 v76, v126, 3, v76
	v_add_u32_e32 v76, 0x8700, v76
	v_lshrrev_b32_e32 v77, 2, v126
	v_mul_u32_u24_e32 v77, 0x104, v77
	v_mul_u32_u24_e32 v125, 0x1040, v128
	v_add_u32_e32 v77, v77, v125
	v_and_b32_e32 v125, 3, v126
	v_lshl_add_u32 v77, v125, 6, v77
	v_add_u32_e32 v77, 0x11000, v77
	s_waitcnt vmcnt(27)
	v_cvt_pk_bf16_f32 v12, v2, v3
	v_cvt_pk_bf16_f32 v13, v4, v5
	ds_write_b64 v124, v[12:13]
	s_waitcnt vmcnt(26)
	v_cvt_pk_bf16_f32 v6, v80, v81
	v_cvt_pk_bf16_f32 v7, v82, v83
	s_and_b32 s13, s2, 7
	s_mul_i32 s14, s13, 0x1100
	v_add_u32_e32 v125, s14, v58
	ds_write_b64 v125, v[6:7]
	s_waitcnt vmcnt(25)
	v_cvt_pk_bf16_f32 v8, v84, v85
	v_cvt_pk_bf16_f32 v9, v86, v87
	s_add_i32 s13, s2, 1
	s_and_b32 s13, s13, 7
	s_mul_i32 s14, s13, 0x1100
	v_add_u32_e32 v10, s14, v58
	ds_write_b64 v10, v[8:9]
	s_waitcnt vmcnt(24)
	v_cvt_pk_bf16_f32 v6, v88, v89
	v_cvt_pk_bf16_f32 v7, v90, v91
	s_add_i32 s13, s2, 2
	s_and_b32 s13, s13, 7
	s_mul_i32 s14, s13, 0x1100
	v_add_u32_e32 v125, s14, v58
	ds_write_b64 v125, v[6:7]
	s_waitcnt vmcnt(23)
	v_cvt_pk_bf16_f32 v8, v92, v93
	v_cvt_pk_bf16_f32 v9, v94, v95
	s_add_i32 s13, s2, 3
	s_and_b32 s13, s13, 7
	s_mul_i32 s14, s13, 0x1100
	v_add_u32_e32 v10, s14, v58
	ds_write_b64 v10, v[8:9]
	s_waitcnt vmcnt(22)
	v_cvt_pk_bf16_f32 v6, v96, v97
	v_cvt_pk_bf16_f32 v7, v98, v99
	s_add_i32 s13, s2, 4
	s_and_b32 s13, s13, 7
	s_mul_i32 s14, s13, 0x1100
	v_add_u32_e32 v125, s14, v58
	ds_write_b64 v125, v[6:7]
	s_waitcnt vmcnt(21)
	v_cvt_pk_bf16_f32 v8, v100, v101
	v_cvt_pk_bf16_f32 v9, v102, v103
	s_add_i32 s13, s2, 5
	s_and_b32 s13, s13, 7
	s_mul_i32 s14, s13, 0x1100
	v_add_u32_e32 v10, s14, v58
	ds_write_b64 v10, v[8:9]
	s_waitcnt vmcnt(20)
	v_cvt_pk_bf16_f32 v6, v108, v109
	v_cvt_pk_bf16_f32 v7, v110, v111
	s_add_i32 s13, s2, 6
	s_and_b32 s13, s13, 7
	s_mul_i32 s14, s13, 0x1100
	v_add_u32_e32 v125, s14, v58
	ds_write_b64 v125, v[6:7]
	s_waitcnt vmcnt(19)
	v_cvt_pk_bf16_f32 v8, v112, v113
	v_cvt_pk_bf16_f32 v9, v114, v115
	s_add_i32 s13, s2, 7
	s_and_b32 s13, s13, 7
	s_mul_i32 s14, s13, 0x1100
	v_add_u32_e32 v10, s14, v58
	ds_write_b64 v10, v[8:9]
	s_waitcnt vmcnt(16)
	v_pk_mul_f32 v[116:117], v[198:199], v[116:117] op_sel_hi:[0,1]
	v_pk_mul_f32 v[118:119], v[198:199], v[118:119] op_sel_hi:[0,1]
	s_waitcnt vmcnt(15)
	v_mul_f32_e32 v6, v117, v133
	v_mul_f32_e32 v7, v119, v135
	v_fmac_f32_e32 v6, v116, v132
	v_fmac_f32_e32 v7, v118, v134
	s_and_b32 s13, s2, 15
	s_mul_i32 s14, s13, 0x104
	s_mul_i32 s15, s13, 0x110
	v_add_f32_e32 v6, v6, v7
	v_add_u32_e32 v125, s14, v59
	ds_write_b32 v125, v6
	v_cvt_pk_bf16_f32 v8, v132, v133
	v_cvt_pk_bf16_f32 v9, v134, v135
	v_add_u32_e32 v10, s15, v76
	s_mov_b64 exec, s[48:49]
	ds_write_b64 v10, v[8:9]
	s_mov_b64 exec, -1
	s_waitcnt vmcnt(14)
	v_mul_f32_e32 v11, v117, v137
	v_mul_f32_e32 v15, v119, v139
	v_fmac_f32_e32 v11, v116, v136
	v_fmac_f32_e32 v15, v118, v138
	s_add_i32 s13, s2, 1
	s_and_b32 s13, s13, 15
	s_mul_i32 s14, s13, 0x104
	s_mul_i32 s15, s13, 0x110
	v_add_f32_e32 v11, v11, v15
	v_add_u32_e32 v16, s14, v59
	ds_write_b32 v16, v11
	v_cvt_pk_bf16_f32 v12, v136, v137
	v_cvt_pk_bf16_f32 v13, v138, v139
	v_add_u32_e32 v14, s15, v76
	s_mov_b64 exec, s[48:49]
	ds_write_b64 v14, v[12:13]
	s_mov_b64 exec, -1
	s_waitcnt vmcnt(13)
	v_mul_f32_e32 v6, v117, v141
	v_mul_f32_e32 v7, v119, v143
	v_fmac_f32_e32 v6, v116, v140
	v_fmac_f32_e32 v7, v118, v142
	s_add_i32 s13, s2, 2
	s_and_b32 s13, s13, 15
	s_mul_i32 s14, s13, 0x104
	s_mul_i32 s15, s13, 0x110
	v_add_f32_e32 v6, v6, v7
	v_add_u32_e32 v125, s14, v59
	ds_write_b32 v125, v6
	v_cvt_pk_bf16_f32 v8, v140, v141
	v_cvt_pk_bf16_f32 v9, v142, v143
	v_add_u32_e32 v10, s15, v76
	s_mov_b64 exec, s[48:49]
	ds_write_b64 v10, v[8:9]
	s_mov_b64 exec, -1
	s_waitcnt vmcnt(12)
	v_mul_f32_e32 v11, v117, v145
	v_mul_f32_e32 v15, v119, v147
	v_fmac_f32_e32 v11, v116, v144
	v_fmac_f32_e32 v15, v118, v146
	s_add_i32 s13, s2, 3
	s_and_b32 s13, s13, 15
	s_mul_i32 s14, s13, 0x104
	s_mul_i32 s15, s13, 0x110
	v_add_f32_e32 v11, v11, v15
	v_add_u32_e32 v16, s14, v59
	ds_write_b32 v16, v11
	v_cvt_pk_bf16_f32 v12, v144, v145
	v_cvt_pk_bf16_f32 v13, v146, v147
	v_add_u32_e32 v14, s15, v76
	s_mov_b64 exec, s[48:49]
	ds_write_b64 v14, v[12:13]
	s_mov_b64 exec, -1
	s_waitcnt vmcnt(11)
	v_mul_f32_e32 v6, v117, v149
	v_mul_f32_e32 v7, v119, v151
	v_fmac_f32_e32 v6, v116, v148
	v_fmac_f32_e32 v7, v118, v150
	s_add_i32 s13, s2, 4
	s_and_b32 s13, s13, 15
	s_mul_i32 s14, s13, 0x104
	s_mul_i32 s15, s13, 0x110
	v_add_f32_e32 v6, v6, v7
	v_add_u32_e32 v125, s14, v59
	ds_write_b32 v125, v6
	v_cvt_pk_bf16_f32 v8, v148, v149
	v_cvt_pk_bf16_f32 v9, v150, v151
	v_add_u32_e32 v10, s15, v76
	s_mov_b64 exec, s[48:49]
	ds_write_b64 v10, v[8:9]
	s_mov_b64 exec, -1
	s_waitcnt vmcnt(10)
	v_mul_f32_e32 v11, v117, v153
	v_mul_f32_e32 v15, v119, v155
	v_fmac_f32_e32 v11, v116, v152
	v_fmac_f32_e32 v15, v118, v154
	s_add_i32 s13, s2, 5
	s_and_b32 s13, s13, 15
	s_mul_i32 s14, s13, 0x104
	s_mul_i32 s15, s13, 0x110
	v_add_f32_e32 v11, v11, v15
	v_add_u32_e32 v16, s14, v59
	ds_write_b32 v16, v11
	v_cvt_pk_bf16_f32 v12, v152, v153
	v_cvt_pk_bf16_f32 v13, v154, v155
	v_add_u32_e32 v14, s15, v76
	s_mov_b64 exec, s[48:49]
	ds_write_b64 v14, v[12:13]
	s_mov_b64 exec, -1
	s_waitcnt vmcnt(9)
	v_mul_f32_e32 v6, v117, v157
	v_mul_f32_e32 v7, v119, v159
	v_fmac_f32_e32 v6, v116, v156
	v_fmac_f32_e32 v7, v118, v158
	s_add_i32 s13, s2, 6
	s_and_b32 s13, s13, 15
	s_mul_i32 s14, s13, 0x104
	s_mul_i32 s15, s13, 0x110
	v_add_f32_e32 v6, v6, v7
	v_add_u32_e32 v125, s14, v59
	ds_write_b32 v125, v6
	v_cvt_pk_bf16_f32 v8, v156, v157
	v_cvt_pk_bf16_f32 v9, v158, v159
	v_add_u32_e32 v10, s15, v76
	s_mov_b64 exec, s[48:49]
	ds_write_b64 v10, v[8:9]
	s_mov_b64 exec, -1
	s_waitcnt vmcnt(8)
	v_mul_f32_e32 v11, v117, v161
	v_mul_f32_e32 v15, v119, v163
	v_fmac_f32_e32 v11, v116, v160
	v_fmac_f32_e32 v15, v118, v162
	s_add_i32 s13, s2, 7
	s_and_b32 s13, s13, 15
	s_mul_i32 s14, s13, 0x104
	s_mul_i32 s15, s13, 0x110
	v_add_f32_e32 v11, v11, v15
	v_add_u32_e32 v16, s14, v59
	ds_write_b32 v16, v11
	v_cvt_pk_bf16_f32 v12, v160, v161
	v_cvt_pk_bf16_f32 v13, v162, v163
	v_add_u32_e32 v14, s15, v76
	s_mov_b64 exec, s[48:49]
	ds_write_b64 v14, v[12:13]
	s_mov_b64 exec, -1
	s_waitcnt vmcnt(7)
	v_mul_f32_e32 v6, v117, v165
	v_mul_f32_e32 v7, v119, v167
	v_fmac_f32_e32 v6, v116, v164
	v_fmac_f32_e32 v7, v118, v166
	s_add_i32 s13, s2, 8
	s_and_b32 s13, s13, 15
	s_mul_i32 s14, s13, 0x104
	s_mul_i32 s15, s13, 0x110
	v_add_f32_e32 v6, v6, v7
	v_add_u32_e32 v125, s14, v59
	ds_write_b32 v125, v6
	v_cvt_pk_bf16_f32 v8, v164, v165
	v_cvt_pk_bf16_f32 v9, v166, v167
	v_add_u32_e32 v10, s15, v76
	s_mov_b64 exec, s[48:49]
	ds_write_b64 v10, v[8:9]
	s_mov_b64 exec, -1
	s_waitcnt vmcnt(6)
	v_mul_f32_e32 v11, v117, v169
	v_mul_f32_e32 v15, v119, v171
	v_fmac_f32_e32 v11, v116, v168
	v_fmac_f32_e32 v15, v118, v170
	s_add_i32 s13, s2, 9
	s_and_b32 s13, s13, 15
	s_mul_i32 s14, s13, 0x104
	s_mul_i32 s15, s13, 0x110
	v_add_f32_e32 v11, v11, v15
	v_add_u32_e32 v16, s14, v59
	ds_write_b32 v16, v11
	v_cvt_pk_bf16_f32 v12, v168, v169
	v_cvt_pk_bf16_f32 v13, v170, v171
	v_add_u32_e32 v14, s15, v76
	s_mov_b64 exec, s[48:49]
	ds_write_b64 v14, v[12:13]
	s_mov_b64 exec, -1
	s_waitcnt vmcnt(5)
	v_mul_f32_e32 v6, v117, v173
	v_mul_f32_e32 v7, v119, v175
	v_fmac_f32_e32 v6, v116, v172
	v_fmac_f32_e32 v7, v118, v174
	s_add_i32 s13, s2, 10
	s_and_b32 s13, s13, 15
	s_mul_i32 s14, s13, 0x104
	s_mul_i32 s15, s13, 0x110
	v_add_f32_e32 v6, v6, v7
	v_add_u32_e32 v125, s14, v59
	ds_write_b32 v125, v6
	v_cvt_pk_bf16_f32 v8, v172, v173
	v_cvt_pk_bf16_f32 v9, v174, v175
	v_add_u32_e32 v10, s15, v76
	s_mov_b64 exec, s[48:49]
	ds_write_b64 v10, v[8:9]
	s_mov_b64 exec, -1
	s_waitcnt vmcnt(4)
	v_mul_f32_e32 v11, v117, v177
	v_mul_f32_e32 v15, v119, v179
	v_fmac_f32_e32 v11, v116, v176
	v_fmac_f32_e32 v15, v118, v178
	s_add_i32 s13, s2, 11
	s_and_b32 s13, s13, 15
	s_mul_i32 s14, s13, 0x104
	s_mul_i32 s15, s13, 0x110
	v_add_f32_e32 v11, v11, v15
	v_add_u32_e32 v16, s14, v59
	ds_write_b32 v16, v11
	v_cvt_pk_bf16_f32 v12, v176, v177
	v_cvt_pk_bf16_f32 v13, v178, v179
	v_add_u32_e32 v14, s15, v76
	s_mov_b64 exec, s[48:49]
	ds_write_b64 v14, v[12:13]
	s_mov_b64 exec, -1
	s_waitcnt vmcnt(3)
	v_mul_f32_e32 v6, v117, v181
	v_mul_f32_e32 v7, v119, v183
	v_fmac_f32_e32 v6, v116, v180
	v_fmac_f32_e32 v7, v118, v182
	s_add_i32 s13, s2, 12
	s_and_b32 s13, s13, 15
	s_mul_i32 s14, s13, 0x104
	s_mul_i32 s15, s13, 0x110
	v_add_f32_e32 v6, v6, v7
	v_add_u32_e32 v125, s14, v59
	ds_write_b32 v125, v6
	v_cvt_pk_bf16_f32 v8, v180, v181
	v_cvt_pk_bf16_f32 v9, v182, v183
	v_add_u32_e32 v10, s15, v76
	s_mov_b64 exec, s[48:49]
	ds_write_b64 v10, v[8:9]
	s_mov_b64 exec, -1
	s_waitcnt vmcnt(2)
	v_mul_f32_e32 v11, v117, v185
	v_mul_f32_e32 v15, v119, v187
	v_fmac_f32_e32 v11, v116, v184
	v_fmac_f32_e32 v15, v118, v186
	s_add_i32 s13, s2, 13
	s_and_b32 s13, s13, 15
	s_mul_i32 s14, s13, 0x104
	s_mul_i32 s15, s13, 0x110
	v_add_f32_e32 v11, v11, v15
	v_add_u32_e32 v16, s14, v59
	ds_write_b32 v16, v11
	v_cvt_pk_bf16_f32 v12, v184, v185
	v_cvt_pk_bf16_f32 v13, v186, v187
	v_add_u32_e32 v14, s15, v76
	s_mov_b64 exec, s[48:49]
	ds_write_b64 v14, v[12:13]
	s_mov_b64 exec, -1
	s_waitcnt vmcnt(1)
	v_mul_f32_e32 v6, v117, v189
	v_mul_f32_e32 v7, v119, v191
	v_fmac_f32_e32 v6, v116, v188
	v_fmac_f32_e32 v7, v118, v190
	s_add_i32 s13, s2, 14
	s_and_b32 s13, s13, 15
	s_mul_i32 s14, s13, 0x104
	s_mul_i32 s15, s13, 0x110
	v_add_f32_e32 v6, v6, v7
	v_add_u32_e32 v125, s14, v59
	ds_write_b32 v125, v6
	v_cvt_pk_bf16_f32 v8, v188, v189
	v_cvt_pk_bf16_f32 v9, v190, v191
	v_add_u32_e32 v10, s15, v76
	s_mov_b64 exec, s[48:49]
	ds_write_b64 v10, v[8:9]
	s_mov_b64 exec, -1
	s_waitcnt vmcnt(0)
	v_mul_f32_e32 v11, v117, v193
	v_mul_f32_e32 v15, v119, v195
	v_fmac_f32_e32 v11, v116, v192
	v_fmac_f32_e32 v15, v118, v194
	s_add_i32 s13, s2, 15
	s_and_b32 s13, s13, 15
	s_mul_i32 s14, s13, 0x104
	s_mul_i32 s15, s13, 0x110
	v_add_f32_e32 v11, v11, v15
	v_add_u32_e32 v16, s14, v59
	ds_write_b32 v16, v11
	v_cvt_pk_bf16_f32 v12, v192, v193
	v_cvt_pk_bf16_f32 v13, v194, v195
	v_add_u32_e32 v14, s15, v76
	s_mov_b64 exec, s[48:49]
	ds_write_b64 v14, v[12:13]
	s_mov_b64 exec, -1
	s_waitcnt lgkmcnt(0)
	ds_read2_b32 v[60:61], v77 offset0:0 offset1:1
	ds_read2_b32 v[62:63], v77 offset0:2 offset1:3
	ds_read2_b32 v[64:65], v77 offset0:4 offset1:5
	ds_read2_b32 v[66:67], v77 offset0:6 offset1:7
	ds_read2_b32 v[68:69], v77 offset0:8 offset1:9
	ds_read2_b32 v[70:71], v77 offset0:10 offset1:11
	ds_read2_b32 v[72:73], v77 offset0:12 offset1:13
	ds_read2_b32 v[74:75], v77 offset0:14 offset1:15
	s_waitcnt lgkmcnt(0)
	v_add_f32_e32 v60, v60, v61
	v_add_f32_e32 v64, v64, v65
	v_add_f32_e32 v68, v68, v69
	v_add_f32_e32 v72, v72, v73
	v_add_f32_e32 v62, v62, v63
	v_add_f32_e32 v66, v66, v67
	v_add_f32_e32 v70, v70, v71
	v_add_f32_e32 v74, v74, v75
	v_add_f32_e32 v60, v60, v62
	v_add_f32_e32 v64, v64, v66
	v_add_f32_e32 v68, v68, v70
	v_add_f32_e32 v72, v72, v74
	v_add_f32_e32 v60, v60, v64
	v_add_f32_e32 v68, v68, v72
	v_add_f32_e32 v78, v60, v68
	s_nop 1
	v_add_f32_dpp v78, v78, v78 quad_perm:[1,0,3,2] row_mask:0xf bank_mask:0xf bound_ctrl:1
	s_nop 1
	v_add_f32_dpp v78, v78, v78 quad_perm:[2,3,0,1] row_mask:0xf bank_mask:0xf bound_ctrl:1
	v_lshlrev_b32_e32 v79, 4, v1
	ds_bpermute_b32 v78, v79, v78
	s_waitcnt lgkmcnt(0)
	s_barrier
	global_load_dwordx4 v[2:5], v123, s[34:35] nt
	global_load_dwordx4 v[6:9], v123, s[34:35] offset:1024 nt
	global_load_dwordx4 v[10:13], v123, s[34:35] offset:2048 nt
	global_load_dwordx4 v[14:17], v123, s[34:35] offset:3072 nt
	ds_read_b128 v[28:31], v53
	ds_read_b128 v[60:63], v56
	ds_read_b128 v[32:35], v53 offset:64
	ds_read_b128 v[64:67], v56 offset:64
	ds_read_b128 v[36:39], v53 offset:128
	ds_read_b128 v[68:71], v56 offset:128
	ds_read_b128 v[40:43], v53 offset:192
	ds_read_b128 v[72:75], v56 offset:192
	s_waitcnt lgkmcnt(6)
	v_mfma_f32_16x16x32_bf16 v[18:21], v[28:31], v[60:63], 0
	s_waitcnt lgkmcnt(4)
	v_mfma_f32_16x16x32_bf16 v[18:21], v[32:35], v[64:67], v[18:21]
	s_waitcnt lgkmcnt(2)
	v_mfma_f32_16x16x32_bf16 v[18:21], v[36:39], v[68:71], v[18:21]
	s_waitcnt lgkmcnt(0)
	v_mfma_f32_16x16x32_bf16 v[18:21], v[40:43], v[72:75], v[18:21]
	ds_read_b128 v[60:63], v57
	ds_read_b128 v[64:67], v57 offset:64
	ds_read_b128 v[68:71], v57 offset:128
	ds_read_b128 v[72:75], v57 offset:192
	s_nop 7
	v_mul_f32_e32 v18, s44, v18
	v_mul_f32_e32 v19, s44, v19
	v_mul_f32_e32 v20, s44, v20
	v_mul_f32_e32 v21, s44, v21
	v_cvt_pk_bf16_f32 v18, v18, v18
	v_cvt_pk_bf16_f32 v19, v19, v19
	v_cvt_pk_bf16_f32 v20, v20, v20
	v_cvt_pk_bf16_f32 v21, v21, v21
	ds_write_b16 v55, v18
	ds_write_b16 v55, v19 offset:272
	ds_write_b16 v55, v20 offset:544
	ds_write_b16 v55, v21 offset:816
	s_waitcnt lgkmcnt(0)
	s_barrier
	ds_read_b128 v[28:31], v54
	ds_read_b128 v[32:35], v54 offset:64
	ds_read_b128 v[36:39], v54 offset:128
	ds_read_b128 v[40:43], v54 offset:192
	s_waitcnt lgkmcnt(3)
	v_mfma_f32_16x16x32_bf16 v[18:21], v[28:31], v[60:63], 0
	s_waitcnt lgkmcnt(2)
	v_mfma_f32_16x16x32_bf16 v[18:21], v[32:35], v[64:67], v[18:21]
	s_waitcnt lgkmcnt(1)
	v_mfma_f32_16x16x32_bf16 v[18:21], v[36:39], v[68:71], v[18:21]
	s_waitcnt lgkmcnt(0)
	v_mfma_f32_16x16x32_bf16 v[18:21], v[40:43], v[72:75], v[18:21]
	s_nop 2
	v_mov_b32_e32 v28, v78
	s_load_dwordx2 s[4:5], s[0:1], 0x70
	v_lshl_or_b32 v30, v24, 2, s3
	v_ashrrev_i32_e32 v31, 31, v30
	v_mov_b32_e32 v107, 0
	s_waitcnt lgkmcnt(0)
	v_add_f32_e32 v34, v130, v28
	v_add_f32_e32 v35, v34, v18
	v_add_f32_e32 v28, v35, v35
	v_mul_f32_e32 v28, 0x3fb8aa3b, v28
	v_exp_f32_e32 v32, v28
	v_lshlrev_b64 v[28:29], 9, v[30:31]
	s_mov_b32 s8, 0x19200
	v_add3_u32 v37, v27, v25, s8
	v_add_f32_e32 v31, 1.0, v32
	v_rcp_f32_e32 v31, v31
	v_lshl_add_u64 v[32:33], s[4:5], 0, v[106:107]
	v_lshl_add_u64 v[28:29], v[32:33], 0, v[28:29]
	global_store_dword v[28:29], v35, off sc1
	v_fma_f32 v35, v31, -2.0, 1.0
	v_fma_f32 v28, -v35, v35, 1.0
	v_mul_f32_e32 v28, v129, v28
	v_add_f32_e32 v31, v34, v19
	v_cvt_pk_bf16_f32 v29, v28, s0
	v_mul_f32_e64 v27, v35, -v28
	v_add_f32_e32 v28, v31, v31
	v_mul_f32_e32 v28, 0x3fb8aa3b, v28
	v_exp_f32_e32 v38, v28
	v_cvt_pk_bf16_f32 v27, v27, s0
	ds_write_b16 v37, v27 offset:4352
	v_or_b32_e32 v28, 1, v30
	v_add_f32_e32 v27, 1.0, v38
	v_rcp_f32_e32 v27, v27
	ds_write_b16 v37, v29
	v_ashrrev_i32_e32 v29, 31, v28
	v_lshlrev_b64 v[28:29], 9, v[28:29]
	v_lshl_add_u64 v[28:29], v[32:33], 0, v[28:29]
	v_fma_f32 v27, v27, -2.0, 1.0
	global_store_dword v[28:29], v31, off sc1
	v_fma_f32 v28, -v27, v27, 1.0
	v_mul_f32_e32 v28, v129, v28
	v_cvt_pk_bf16_f32 v29, v28, s0
	v_add_f32_e32 v31, v34, v20
	ds_write_b16 v37, v29 offset:272
	v_add_f32_e32 v29, v31, v31
	v_mul_f32_e32 v29, 0x3fb8aa3b, v29
	v_exp_f32_e32 v38, v29
	v_mul_f32_e64 v28, v27, -v28
	v_cvt_pk_bf16_f32 v28, v28, s0
	ds_write_b16 v37, v28 offset:4624
	v_add_f32_e32 v38, 1.0, v38
	v_or_b32_e32 v28, 2, v30
	v_rcp_f32_e32 v38, v38
	v_ashrrev_i32_e32 v29, 31, v28
	v_lshlrev_b64 v[28:29], 9, v[28:29]
	v_lshl_add_u64 v[28:29], v[32:33], 0, v[28:29]
	global_store_dword v[28:29], v31, off sc1
	v_fma_f32 v28, v38, -2.0, 1.0
	v_fma_f32 v29, -v28, v28, 1.0
	v_mul_f32_e32 v29, v129, v29
	v_cvt_pk_bf16_f32 v31, v29, s0
	v_add_f32_e32 v34, v34, v21
	ds_write_b16 v37, v31 offset:544
	v_add_f32_e32 v31, v34, v34
	v_mul_f32_e32 v31, 0x3fb8aa3b, v31
	v_exp_f32_e32 v38, v31
	v_mul_f32_e64 v29, v28, -v29
	v_cvt_pk_bf16_f32 v29, v29, s0
	ds_write_b16 v37, v29 offset:4896
	v_add_f32_e32 v29, 1.0, v38
	v_rcp_f32_e32 v29, v29
	v_or_b32_e32 v30, 3, v30
	v_ashrrev_i32_e32 v31, 31, v30
	v_lshlrev_b64 v[30:31], 9, v[30:31]
	v_lshl_add_u64 v[30:31], v[32:33], 0, v[30:31]
	v_fma_f32 v29, v29, -2.0, 1.0
	global_store_dword v[30:31], v34, off sc1
	v_fma_f32 v30, -v29, v29, 1.0
	v_mul_f32_e32 v30, v129, v30
	v_cvt_pk_bf16_f32 v31, v30, s0
	v_mul_f32_e64 v30, v29, -v30
	v_cvt_pk_bf16_f32 v30, v30, s0
	ds_write_b16 v37, v30 offset:5168
	v_mov_b32_e32 v30, 0x1d800
	v_mul_f32_e32 v36, v129, v35
	v_lshl_or_b32 v32, v128, 6, v30
	v_mov_b32_e32 v30, v107
	ds_write_b16 v37, v31 offset:816
	v_mov_b32_e32 v31, 0
	v_mov_b32_dpp v30, v36 quad_perm:[1,0,3,2] row_mask:0xf bank_mask:0xf
	v_fmac_f32_e32 v30, v129, v35
	v_cmp_eq_u32_e32 vcc, 0, v1
	v_add_u32_e32 v26, v32, v26
	v_add_f32_dpp v30, v30, v30 quad_perm:[2,3,0,1] row_mask:0xf bank_mask:0xf bound_ctrl:1
	s_nop 1
	v_add_f32_dpp v30, v30, v30 row_half_mirror row_mask:0xf bank_mask:0xf bound_ctrl:1
	s_nop 1
	v_mov_b32_dpp v31, v30 row_mirror row_mask:0xf bank_mask:0xf
	s_and_saveexec_b64 s[4:5], vcc
	v_add_f32_e32 v30, v30, v31
	ds_write_b32 v26, v30
	s_or_b64 exec, exec, s[4:5]
	v_mul_f32_e32 v30, v129, v27
	v_mov_b32_e32 v31, 0
	s_nop 1
	v_mov_b32_dpp v31, v30 quad_perm:[1,0,3,2] row_mask:0xf bank_mask:0xf
	v_fmac_f32_e32 v31, v129, v27
	s_nop 1
	v_add_f32_dpp v27, v31, v31 quad_perm:[2,3,0,1] row_mask:0xf bank_mask:0xf bound_ctrl:1
	s_nop 1
	v_add_f32_dpp v27, v27, v27 row_half_mirror row_mask:0xf bank_mask:0xf bound_ctrl:1
	s_nop 1
	v_mov_b32_dpp v107, v27 row_mirror row_mask:0xf bank_mask:0xf
	s_and_saveexec_b64 s[4:5], vcc
	v_add_f32_e32 v27, v27, v107
	ds_write_b32 v26, v27 offset:4
	s_or_b64 exec, exec, s[4:5]
	v_mul_f32_e32 v30, v129, v28
	v_mov_b32_e32 v31, 0
	v_mov_b32_e32 v27, 0
	s_nop 0
	v_mov_b32_dpp v31, v30 quad_perm:[1,0,3,2] row_mask:0xf bank_mask:0xf
	v_fmac_f32_e32 v31, v129, v28
	v_mov_b32_e32 v30, 0
	s_nop 0
	v_add_f32_dpp v28, v31, v31 quad_perm:[2,3,0,1] row_mask:0xf bank_mask:0xf bound_ctrl:1
	s_nop 1
	v_add_f32_dpp v28, v28, v28 row_half_mirror row_mask:0xf bank_mask:0xf bound_ctrl:1
	s_nop 1
	v_mov_b32_dpp v30, v28 row_mirror row_mask:0xf bank_mask:0xf
	s_and_saveexec_b64 s[4:5], vcc
	v_add_f32_e32 v28, v28, v30
	ds_write_b32 v26, v28 offset:8
	s_or_b64 exec, exec, s[4:5]
	v_mul_f32_e32 v28, v129, v29
	v_mov_b32_e32 v30, 0
	s_nop 1
	v_mov_b32_dpp v30, v28 quad_perm:[1,0,3,2] row_mask:0xf bank_mask:0xf
	v_fmac_f32_e32 v30, v129, v29
	s_nop 1
	v_add_f32_dpp v28, v30, v30 quad_perm:[2,3,0,1] row_mask:0xf bank_mask:0xf bound_ctrl:1
	s_nop 1
	v_add_f32_dpp v28, v28, v28 row_half_mirror row_mask:0xf bank_mask:0xf bound_ctrl:1
	s_nop 1
	v_mov_b32_dpp v27, v28 row_mirror row_mask:0xf bank_mask:0xf
	s_and_saveexec_b64 s[4:5], vcc
	v_add_f32_e32 v27, v28, v27
	ds_write_b32 v26, v27 offset:12
	s_or_b64 exec, exec, s[4:5]
	s_mov_b64 s[4:5], 0
	s_branch .LBB0_28
.Lp_q:
	v_lshrrev_b32_e32 v122, 5, v0
	v_lshlrev_b32_e32 v122, 10, v122
	v_and_b32_e32 v125, 31, v0
	v_lshl_add_u32 v122, v125, 4, v122
	s_and_b32 s13, s2, 7
	s_lshl_b32 s14, s13, 14
	v_add_u32_e32 v125, s14, v122
	global_load_dwordx4 v[132:135], v125, s[28:29]
	s_add_i32 s13, s2, 1
	s_and_b32 s13, s13, 7
	s_lshl_b32 s14, s13, 14
	v_add_u32_e32 v125, s14, v122
	global_load_dwordx4 v[136:139], v125, s[28:29]
	s_add_i32 s13, s2, 2
	s_and_b32 s13, s13, 7
	s_lshl_b32 s14, s13, 14
	v_add_u32_e32 v125, s14, v122
	global_load_dwordx4 v[140:143], v125, s[28:29]
	s_add_i32 s13, s2, 3
	s_and_b32 s13, s13, 7
	s_lshl_b32 s14, s13, 14
	v_add_u32_e32 v125, s14, v122
	global_load_dwordx4 v[144:147], v125, s[28:29]
	s_add_i32 s13, s2, 4
	s_and_b32 s13, s13, 7
	s_lshl_b32 s14, s13, 14
	v_add_u32_e32 v125, s14, v122
	global_load_dwordx4 v[148:151], v125, s[28:29]
	s_add_i32 s13, s2, 5
	s_and_b32 s13, s13, 7
	s_lshl_b32 s14, s13, 14
	v_add_u32_e32 v125, s14, v122
	global_load_dwordx4 v[152:155], v125, s[28:29]
	s_add_i32 s13, s2, 6
	s_and_b32 s13, s13, 7
	s_lshl_b32 s14, s13, 14
	v_add_u32_e32 v125, s14, v122
	global_load_dwordx4 v[156:159], v125, s[28:29]
	s_add_i32 s13, s2, 7
	s_and_b32 s13, s13, 7
	s_lshl_b32 s14, s13, 14
	v_add_u32_e32 v125, s14, v122
	global_load_dwordx4 v[160:163], v125, s[28:29]
	s_waitcnt vmcnt(18)
	v_cvt_pk_bf16_f32 v12, v2, v3
	v_cvt_pk_bf16_f32 v13, v4, v5
	ds_write_b64 v124, v[12:13]
	s_waitcnt vmcnt(17)
	v_cvt_pk_bf16_f32 v6, v80, v81
	v_cvt_pk_bf16_f32 v7, v82, v83
	s_and_b32 s13, s2, 7
	s_mul_i32 s14, s13, 0x1100
	v_add_u32_e32 v125, s14, v58
	ds_write_b64 v125, v[6:7]
	s_waitcnt vmcnt(16)
	v_cvt_pk_bf16_f32 v8, v84, v85
	v_cvt_pk_bf16_f32 v9, v86, v87
	s_add_i32 s13, s2, 1
	s_and_b32 s13, s13, 7
	s_mul_i32 s14, s13, 0x1100
	v_add_u32_e32 v10, s14, v58
	ds_write_b64 v10, v[8:9]
	s_waitcnt vmcnt(15)
	v_cvt_pk_bf16_f32 v6, v88, v89
	v_cvt_pk_bf16_f32 v7, v90, v91
	s_add_i32 s13, s2, 2
	s_and_b32 s13, s13, 7
	s_mul_i32 s14, s13, 0x1100
	v_add_u32_e32 v125, s14, v58
	ds_write_b64 v125, v[6:7]
	s_waitcnt vmcnt(14)
	v_cvt_pk_bf16_f32 v8, v92, v93
	v_cvt_pk_bf16_f32 v9, v94, v95
	s_add_i32 s13, s2, 3
	s_and_b32 s13, s13, 7
	s_mul_i32 s14, s13, 0x1100
	v_add_u32_e32 v10, s14, v58
	ds_write_b64 v10, v[8:9]
	s_waitcnt vmcnt(13)
	v_cvt_pk_bf16_f32 v6, v96, v97
	v_cvt_pk_bf16_f32 v7, v98, v99
	s_add_i32 s13, s2, 4
	s_and_b32 s13, s13, 7
	s_mul_i32 s14, s13, 0x1100
	v_add_u32_e32 v125, s14, v58
	ds_write_b64 v125, v[6:7]
	s_waitcnt vmcnt(12)
	v_cvt_pk_bf16_f32 v8, v100, v101
	v_cvt_pk_bf16_f32 v9, v102, v103
	s_add_i32 s13, s2, 5
	s_and_b32 s13, s13, 7
	s_mul_i32 s14, s13, 0x1100
	v_add_u32_e32 v10, s14, v58
	ds_write_b64 v10, v[8:9]
	s_waitcnt vmcnt(11)
	v_cvt_pk_bf16_f32 v6, v108, v109
	v_cvt_pk_bf16_f32 v7, v110, v111
	s_add_i32 s13, s2, 6
	s_and_b32 s13, s13, 7
	s_mul_i32 s14, s13, 0x1100
	v_add_u32_e32 v125, s14, v58
	ds_write_b64 v125, v[6:7]
	s_waitcnt vmcnt(10)
	v_cvt_pk_bf16_f32 v8, v112, v113
	v_cvt_pk_bf16_f32 v9, v114, v115
	s_add_i32 s13, s2, 7
	s_and_b32 s13, s13, 7
	s_mul_i32 s14, s13, 0x1100
	v_add_u32_e32 v10, s14, v58
	ds_write_b64 v10, v[8:9]
	s_waitcnt vmcnt(7)
	v_cvt_pk_bf16_f32 v6, v132, v133
	v_cvt_pk_bf16_f32 v7, v134, v135
	s_and_b32 s13, s2, 7
	s_mul_i32 s14, s13, 0x1100
	s_add_i32 s14, s14, 34816
	v_add_u32_e32 v125, s14, v58
	ds_write_b64 v125, v[6:7]
	s_waitcnt vmcnt(6)
	v_cvt_pk_bf16_f32 v8, v136, v137
	v_cvt_pk_bf16_f32 v9, v138, v139
	s_add_i32 s13, s2, 1
	s_and_b32 s13, s13, 7
	s_mul_i32 s14, s13, 0x1100
	s_add_i32 s14, s14, 34816
	v_add_u32_e32 v10, s14, v58
	ds_write_b64 v10, v[8:9]
	s_waitcnt vmcnt(5)
	v_cvt_pk_bf16_f32 v6, v140, v141
	v_cvt_pk_bf16_f32 v7, v142, v143
	s_add_i32 s13, s2, 2
	s_and_b32 s13, s13, 7
	s_mul_i32 s14, s13, 0x1100
	s_add_i32 s14, s14, 34816
	v_add_u32_e32 v125, s14, v58
	ds_write_b64 v125, v[6:7]
	s_waitcnt vmcnt(4)
	v_cvt_pk_bf16_f32 v8, v144, v145
	v_cvt_pk_bf16_f32 v9, v146, v147
	s_add_i32 s13, s2, 3
	s_and_b32 s13, s13, 7
	s_mul_i32 s14, s13, 0x1100
	s_add_i32 s14, s14, 34816
	v_add_u32_e32 v10, s14, v58
	ds_write_b64 v10, v[8:9]
	s_waitcnt vmcnt(3)
	v_cvt_pk_bf16_f32 v6, v148, v149
	v_cvt_pk_bf16_f32 v7, v150, v151
	s_add_i32 s13, s2, 4
	s_and_b32 s13, s13, 7
	s_mul_i32 s14, s13, 0x1100
	s_add_i32 s14, s14, 34816
	v_add_u32_e32 v125, s14, v58
	ds_write_b64 v125, v[6:7]
	s_waitcnt vmcnt(2)
	v_cvt_pk_bf16_f32 v8, v152, v153
	v_cvt_pk_bf16_f32 v9, v154, v155
	s_add_i32 s13, s2, 5
	s_and_b32 s13, s13, 7
	s_mul_i32 s14, s13, 0x1100
	s_add_i32 s14, s14, 34816
	v_add_u32_e32 v10, s14, v58
	ds_write_b64 v10, v[8:9]
	s_waitcnt vmcnt(1)
	v_cvt_pk_bf16_f32 v6, v156, v157
	v_cvt_pk_bf16_f32 v7, v158, v159
	s_add_i32 s13, s2, 6
	s_and_b32 s13, s13, 7
	s_mul_i32 s14, s13, 0x1100
	s_add_i32 s14, s14, 34816
	v_add_u32_e32 v125, s14, v58
	ds_write_b64 v125, v[6:7]
	s_waitcnt vmcnt(0)
	v_cvt_pk_bf16_f32 v8, v160, v161
	v_cvt_pk_bf16_f32 v9, v162, v163
	s_add_i32 s13, s2, 7
	s_and_b32 s13, s13, 7
	s_mul_i32 s14, s13, 0x1100
	s_add_i32 s14, s14, 34816
	v_add_u32_e32 v10, s14, v58
	ds_write_b64 v10, v[8:9]
	s_waitcnt lgkmcnt(0)
	s_barrier
	global_load_dwordx4 v[2:5], v123, s[34:35] nt
	global_load_dwordx4 v[6:9], v123, s[34:35] offset:1024 nt
	global_load_dwordx4 v[10:13], v123, s[34:35] offset:2048 nt
	global_load_dwordx4 v[14:17], v123, s[34:35] offset:3072 nt
	ds_read_b128 v[28:31], v53
	ds_read_b128 v[60:63], v56
	ds_read_b128 v[32:35], v53 offset:64
	ds_read_b128 v[64:67], v56 offset:64
	ds_read_b128 v[36:39], v53 offset:128
	ds_read_b128 v[68:71], v56 offset:128
	ds_read_b128 v[40:43], v53 offset:192
	ds_read_b128 v[72:75], v56 offset:192
	s_waitcnt lgkmcnt(6)
	v_mfma_f32_16x16x32_bf16 v[18:21], v[28:31], v[60:63], 0
	s_waitcnt lgkmcnt(4)
	v_mfma_f32_16x16x32_bf16 v[18:21], v[32:35], v[64:67], v[18:21]
	s_waitcnt lgkmcnt(2)
	v_mfma_f32_16x16x32_bf16 v[18:21], v[36:39], v[68:71], v[18:21]
	s_waitcnt lgkmcnt(0)
	v_mfma_f32_16x16x32_bf16 v[18:21], v[40:43], v[72:75], v[18:21]
	ds_read_b128 v[60:63], v57
	ds_read_b128 v[64:67], v57 offset:64
	ds_read_b128 v[68:71], v57 offset:128
	ds_read_b128 v[72:75], v57 offset:192
	s_nop 7
	v_mul_f32_e32 v18, s44, v18
	v_mul_f32_e32 v19, s44, v19
	v_mul_f32_e32 v20, s44, v20
	v_mul_f32_e32 v21, s44, v21
	v_cvt_pk_bf16_f32 v18, v18, v18
	v_cvt_pk_bf16_f32 v19, v19, v19
	v_cvt_pk_bf16_f32 v20, v20, v20
	v_cvt_pk_bf16_f32 v21, v21, v21
	ds_write_b16 v55, v18
	ds_write_b16 v55, v19 offset:272
	ds_write_b16 v55, v20 offset:544
	ds_write_b16 v55, v21 offset:816
	s_waitcnt lgkmcnt(0)
	s_barrier
	ds_read_b128 v[28:31], v54
	ds_read_b128 v[32:35], v54 offset:64
	ds_read_b128 v[36:39], v54 offset:128
	ds_read_b128 v[40:43], v54 offset:192
	s_waitcnt lgkmcnt(3)
	v_mfma_f32_16x16x32_bf16 v[18:21], v[28:31], v[60:63], 0
	s_waitcnt lgkmcnt(2)
	v_mfma_f32_16x16x32_bf16 v[18:21], v[32:35], v[64:67], v[18:21]
	s_waitcnt lgkmcnt(1)
	v_mfma_f32_16x16x32_bf16 v[18:21], v[36:39], v[68:71], v[18:21]
	s_waitcnt lgkmcnt(0)
	v_mfma_f32_16x16x32_bf16 v[18:21], v[40:43], v[72:75], v[18:21]
	s_load_dwordx2 s[4:5], s[0:1], 0x68
	v_lshl_or_b32 v26, v24, 2, s12
	v_mov_b32_e32 v107, 0
	v_ashrrev_i32_e32 v27, 31, v26
	v_lshlrev_b64 v[28:29], 9, v[26:27]
	s_waitcnt lgkmcnt(0)
	v_lshl_add_u64 v[30:31], s[4:5], 0, v[106:107]
	v_lshl_add_u64 v[28:29], v[30:31], 0, v[28:29]
	v_mul_u32_u24_e32 v24, 0x440, v24
	s_mov_b32 s4, 0x19200
	global_store_dword v[28:29], v18, off sc1
	v_add3_u32 v28, v24, v25, s4
	v_mul_f32_e32 v24, v18, v18
	v_cvt_pk_bf16_f32 v27, v18, s0
	v_cvt_pk_bf16_f32 v24, v24, s0
	ds_write_b16 v28, v27
	ds_write_b16 v28, v24 offset:4352
	v_max3_f32 v27, |v18|, 0, |v19|
	v_or_b32_e32 v24, 1, v26
	v_cvt_pk_bf16_f32 v18, v19, s0
	v_ashrrev_i32_e32 v25, 31, v24
	ds_write_b16 v28, v18 offset:272
	v_mul_f32_e32 v18, v19, v19
	v_lshlrev_b64 v[24:25], 9, v[24:25]
	v_cvt_pk_bf16_f32 v18, v18, s0
	v_lshl_add_u64 v[24:25], v[30:31], 0, v[24:25]
	ds_write_b16 v28, v18 offset:4624
	v_or_b32_e32 v18, 2, v26
	global_store_dword v[24:25], v19, off sc1
	v_ashrrev_i32_e32 v19, 31, v18
	v_lshlrev_b64 v[18:19], 9, v[18:19]
	v_lshl_add_u64 v[18:19], v[30:31], 0, v[18:19]
	global_store_dword v[18:19], v20, off sc1
	v_cvt_pk_bf16_f32 v18, v20, s0
	ds_write_b16 v28, v18 offset:544
	v_mul_f32_e32 v18, v20, v20
	v_cvt_pk_bf16_f32 v18, v18, s0
	ds_write_b16 v28, v18 offset:4896
	v_or_b32_e32 v18, 3, v26
	v_ashrrev_i32_e32 v19, 31, v18
	v_lshlrev_b64 v[18:19], 9, v[18:19]
	v_lshl_add_u64 v[18:19], v[30:31], 0, v[18:19]
	global_store_dword v[18:19], v21, off sc1
	v_cvt_pk_bf16_f32 v18, v21, s0
	ds_write_b16 v28, v18 offset:816
	v_mul_f32_e32 v18, v21, v21
	v_cvt_pk_bf16_f32 v18, v18, s0
	v_max3_f32 v20, v27, |v20|, |v21|
	ds_write_b16 v28, v18 offset:5168
	v_mov_b32_e32 v18, v107
	v_mov_b32_e32 v19, v107
	v_cmp_eq_u32_e32 vcc, 0, v126
	v_mov_b32_dpp v18, v20 quad_perm:[1,0,3,2] row_mask:0xf bank_mask:0xf
	v_max_f32_e32 v18, v18, v18
	v_max_f32_e32 v18, v20, v18
	s_nop 1
	v_mov_b32_dpp v19, v18 quad_perm:[2,3,0,1] row_mask:0xf bank_mask:0xf
	v_max_f32_e32 v19, v19, v19
	v_max_f32_e32 v18, v18, v19
	v_mov_b32_e32 v19, v107
	s_nop 1
	v_mov_b32_dpp v19, v18 row_half_mirror row_mask:0xf bank_mask:0xf
	v_max_f32_e32 v19, v19, v19
	v_max_f32_e32 v18, v18, v19
	v_mov_b32_e32 v19, v107
	s_nop 1
	v_mov_b32_dpp v19, v18 row_mirror row_mask:0xf bank_mask:0xf
	v_max_f32_e32 v19, v19, v19
	v_max_f32_e32 v18, v18, v19
	s_nop 0
	v_readlane_b32 s8, v18, 0
	v_readlane_b32 s9, v18, 16
	v_readlane_b32 s10, v18, 32
	v_readlane_b32 s11, v18, 48
	v_and_b32_e32 v18, 0x7fffffff, v129
	s_nop 1
	v_add_f32_dpp v18, v18, |v129| quad_perm:[1,0,3,2] row_mask:0xf bank_mask:0xf bound_ctrl:1
	s_nop 1
	v_add_f32_dpp v18, v18, v18 quad_perm:[2,3,0,1] row_mask:0xf bank_mask:0xf bound_ctrl:1
	s_nop 1
	v_add_f32_dpp v18, v18, v18 row_half_mirror row_mask:0xf bank_mask:0xf bound_ctrl:1
	s_nop 1
	v_mov_b32_dpp v107, v18 row_mirror row_mask:0xf bank_mask:0xf
	s_and_saveexec_b64 s[4:5], vcc
	s_cbranch_execz .LBB0_27
	v_mov_b32_e32 v19, 0x1d800
	v_lshl_or_b32 v20, v128, 6, v19
	v_add_f32_e32 v19, v18, v107
	v_max_f32_e64 v18, s11, s11
	v_max_f32_e64 v21, s10, s10
	v_max_f32_e32 v18, v21, v18
	v_mov_b32_e32 v21, s9
	v_max3_f32 v18, s8, v21, v18
	ds_write_b64 v20, v[18:19]
